# topk stage 2: key->float and+xor pairs fused into v_bitop3_b32 (14 of 16)
# speedup vs baseline: 1.0008x; 1.0008x over previous
.LBB0_1854:
	s_mov_b32 s98, 0x7fffffff
	v_cndmask_b32_e64 v153, 0, v153, s[0:1]
	v_cndmask_b32_e64 v154, 0, v154, s[0:1]
	v_cndmask_b32_e64 v153, v153, v157, s[54:55]
	v_cndmask_b32_e64 v155, 0, v155, s[0:1]
	v_cndmask_b32_e64 v154, v154, v158, s[54:55]
	v_cndmask_b32_e64 v153, v153, v161, s[64:65]
	v_cndmask_b32_e64 v155, v155, v159, s[54:55]
	v_cndmask_b32_e64 v154, v154, v162, s[64:65]
	v_cndmask_b32_e64 v153, v153, v165, s[2:3]
	v_cndmask_b32_e64 v155, v155, v163, s[64:65]
	v_cndmask_b32_e64 v154, v154, v166, s[2:3]
	v_cndmask_b32_e64 v153, v153, v169, s[6:7]
	v_cndmask_b32_e64 v155, v155, v167, s[2:3]
	v_cndmask_b32_e64 v154, v154, v170, s[6:7]
	v_cndmask_b32_e64 v153, v153, v173, s[96:97]
	v_cndmask_b32_e64 v156, 0, v156, s[0:1]
	v_cndmask_b32_e64 v155, v155, v171, s[6:7]
	v_cndmask_b32_e64 v154, v154, v174, s[96:97]
	v_cndmask_b32_e64 v153, v153, v177, s[66:67]
	v_cndmask_b32_e64 v156, v156, v160, s[54:55]
	v_cndmask_b32_e64 v155, v155, v175, s[96:97]
	v_cndmask_b32_e64 v154, v154, v178, s[66:67]
	v_cndmask_b32_e64 v153, v153, v181, s[24:25]
	v_cndmask_b32_e64 v156, v156, v164, s[64:65]
	v_cndmask_b32_e64 v155, v155, v179, s[66:67]
	v_cndmask_b32_e64 v154, v154, v182, s[24:25]
	v_cndmask_b32_e64 v153, v153, v185, s[26:27]
	v_cndmask_b32_e64 v156, v156, v168, s[2:3]
	v_cndmask_b32_e64 v155, v155, v183, s[24:25]
	v_cndmask_b32_e64 v154, v154, v186, s[26:27]
	v_cndmask_b32_e64 v153, v153, v189, s[28:29]
	v_cndmask_b32_e64 v156, v156, v172, s[6:7]
	v_cndmask_b32_e64 v155, v155, v187, s[26:27]
	v_cndmask_b32_e64 v154, v154, v190, s[28:29]
	v_cndmask_b32_e64 v153, v153, v193, s[30:31]
	v_cndmask_b32_e64 v156, v156, v176, s[96:97]
	v_cndmask_b32_e64 v155, v155, v191, s[28:29]
	v_cndmask_b32_e64 v154, v154, v194, s[30:31]
	v_cndmask_b32_e64 v153, v153, v197, s[34:35]
	v_cndmask_b32_e64 v156, v156, v180, s[66:67]
	v_cndmask_b32_e64 v155, v155, v195, s[30:31]
	v_cndmask_b32_e64 v154, v154, v198, s[34:35]
	v_cndmask_b32_e64 v153, v153, v206, s[36:37]
	v_cndmask_b32_e64 v156, v156, v184, s[24:25]
	v_cndmask_b32_e64 v155, v155, v199, s[34:35]
	v_cndmask_b32_e64 v154, v154, v207, s[36:37]
	v_cndmask_b32_e64 v153, v153, v210, s[38:39]
	v_cndmask_b32_e64 v156, v156, v188, s[26:27]
	v_cndmask_b32_e64 v155, v155, v208, s[36:37]
	v_cndmask_b32_e64 v154, v154, v211, s[38:39]
	v_cndmask_b32_e64 v153, v153, v214, s[40:41]
	v_max_i32_e32 v157, v218, v219
	v_cndmask_b32_e64 v156, v156, v192, s[28:29]
	v_cndmask_b32_e64 v155, v155, v212, s[38:39]
	v_cndmask_b32_e64 v154, v154, v215, s[40:41]
	v_cndmask_b32_e64 v153, v153, v157, s[42:43]
	v_max_i32_e32 v157, v220, v221
	v_cndmask_b32_e64 v156, v156, v196, s[30:31]
	v_cndmask_b32_e64 v155, v155, v216, s[40:41]
	v_cndmask_b32_e64 v157, v154, v157, s[42:43]
	v_max_i32_e32 v154, v240, v241
	ds_bpermute_b32 v158, v146, v153
	v_cndmask_b32_e64 v156, v156, v203, s[34:35]
	v_cndmask_b32_e64 v159, v155, v154, s[42:43]
	ds_bpermute_b32 v154, v147, v153
	v_cndmask_b32_e64 v156, v156, v209, s[36:37]
	v_cndmask_b32_e64 v156, v156, v213, s[38:39]
	v_cndmask_b32_e64 v156, v156, v217, s[40:41]
	v_max_i32_e32 v155, v222, v223
	v_cndmask_b32_e64 v167, v156, v155, s[42:43]
	s_waitcnt lgkmcnt(1)
	v_lshlrev_b32_e32 v155, 7, v158
	v_and_b32_e32 v155, 0x3f80, v155
	s_waitcnt lgkmcnt(0)
	v_and_b32_e32 v156, 0x7f, v154
	s_movk_i32 s9, 0x3fff
	v_bitop3_b32 v184, v156, s9, v155 bitop3:0x36
	v_ashrrev_i32_e32 v155, 31, v154
	v_ashrrev_i32_e32 v156, 31, v158
	s_nop 0
	s_nop 0
	v_bitop3_b32 v155, v155, v154, s98 bitop3:0x6c
	v_bitop3_b32 v154, v156, v158, s98 bitop3:0x6c
	ds_bpermute_b32 v156, v148, v153
	ds_bpermute_b32 v153, v149, v153
	v_pk_add_f32 v[154:155], v[154:155], v[154:155] op_sel:[1,0] op_sel_hi:[0,1]
	s_movk_i32 s10, 0xffc0
	v_and_or_b32 v154, v154, s10, v141
	v_cndmask_b32_e64 v185, v238, v154, s[4:5]
	s_waitcnt lgkmcnt(1)
	v_lshlrev_b32_e32 v154, 7, v156
	v_and_b32_e32 v154, 0x3f80, v154
	s_waitcnt lgkmcnt(0)
	v_and_b32_e32 v155, 0x7f, v153
	v_bitop3_b32 v166, v155, s9, v154 bitop3:0x36
	v_ashrrev_i32_e32 v154, 31, v153
	v_ashrrev_i32_e32 v155, 31, v156
	s_nop 0
	v_and_b32_e32 v158, 0x7fffffff, v155
	v_bitop3_b32 v155, v154, v153, s98 bitop3:0x6c
	v_xor_b32_e32 v154, v158, v156
	v_pk_add_f32 v[154:155], v[154:155], v[154:155] op_sel:[1,0] op_sel_hi:[0,1]
	ds_bpermute_b32 v153, v146, v157
	ds_bpermute_b32 v155, v147, v157
	v_and_or_b32 v154, v154, s10, v141
	v_cndmask_b32_e64 v186, v238, v154, s[4:5]
	ds_bpermute_b32 v187, v149, v167
	s_waitcnt lgkmcnt(2)
	v_lshlrev_b32_e32 v154, 7, v153
	v_and_b32_e32 v154, 0x3f80, v154
	s_waitcnt lgkmcnt(1)
	v_and_b32_e32 v156, 0x7f, v155
	v_bitop3_b32 v164, v156, s9, v154 bitop3:0x36
	v_ashrrev_i32_e32 v154, 31, v155
	v_ashrrev_i32_e32 v156, 31, v153
	s_nop 0
	s_nop 0
	v_bitop3_b32 v155, v154, v155, s98 bitop3:0x6c
	v_bitop3_b32 v154, v156, v153, s98 bitop3:0x6c
	ds_bpermute_b32 v153, v148, v157
	v_pk_add_f32 v[154:155], v[154:155], v[154:155] op_sel:[1,0] op_sel_hi:[0,1]
	ds_bpermute_b32 v155, v149, v157
	v_and_or_b32 v154, v154, s10, v141
	v_cndmask_b32_e64 v165, v238, v154, s[4:5]
	s_waitcnt lgkmcnt(1)
	v_lshlrev_b32_e32 v154, 7, v153
	v_and_b32_e32 v154, 0x3f80, v154
	s_waitcnt lgkmcnt(0)
	v_and_b32_e32 v156, 0x7f, v155
	v_bitop3_b32 v162, v156, s9, v154 bitop3:0x36
	v_ashrrev_i32_e32 v154, 31, v155
	v_ashrrev_i32_e32 v156, 31, v153
	s_nop 0
	s_nop 0
	v_bitop3_b32 v155, v154, v155, s98 bitop3:0x6c
	v_bitop3_b32 v154, v156, v153, s98 bitop3:0x6c
	v_pk_add_f32 v[154:155], v[154:155], v[154:155] op_sel:[1,0] op_sel_hi:[0,1]
	ds_bpermute_b32 v153, v146, v159
	ds_bpermute_b32 v155, v147, v159
	v_and_or_b32 v154, v154, s10, v141
	v_cndmask_b32_e64 v163, v238, v154, s[4:5]
	ds_write2st64_b32 v142, v185, v186 offset1:1
	s_waitcnt lgkmcnt(2)
	v_lshlrev_b32_e32 v154, 7, v153
	v_and_b32_e32 v154, 0x3f80, v154
	s_waitcnt lgkmcnt(1)
	v_and_b32_e32 v156, 0x7f, v155
	v_bitop3_b32 v160, v156, s9, v154 bitop3:0x36
	v_ashrrev_i32_e32 v154, 31, v155
	v_ashrrev_i32_e32 v156, 31, v153
	s_nop 0
	s_nop 0
	v_bitop3_b32 v155, v154, v155, s98 bitop3:0x6c
	v_bitop3_b32 v154, v156, v153, s98 bitop3:0x6c
	ds_bpermute_b32 v153, v148, v159
	v_pk_add_f32 v[154:155], v[154:155], v[154:155] op_sel:[1,0] op_sel_hi:[0,1]
	ds_bpermute_b32 v155, v149, v159
	v_and_or_b32 v154, v154, s10, v141
	v_cndmask_b32_e64 v161, v238, v154, s[4:5]
	s_waitcnt lgkmcnt(1)
	v_lshlrev_b32_e32 v154, 7, v153
	v_and_b32_e32 v154, 0x3f80, v154
	s_waitcnt lgkmcnt(0)
	v_and_b32_e32 v156, 0x7f, v155
	v_bitop3_b32 v158, v156, s9, v154 bitop3:0x36
	v_ashrrev_i32_e32 v154, 31, v155
	v_ashrrev_i32_e32 v156, 31, v153
	s_nop 0
	s_nop 0
	v_bitop3_b32 v155, v154, v155, s98 bitop3:0x6c
	v_bitop3_b32 v154, v156, v153, s98 bitop3:0x6c
	ds_bpermute_b32 v153, v146, v167
	ds_bpermute_b32 v156, v147, v167
	v_pk_add_f32 v[154:155], v[154:155], v[154:155] op_sel:[1,0] op_sel_hi:[0,1]
	v_and_or_b32 v154, v154, s10, v141
	v_cndmask_b32_e64 v159, v238, v154, s[4:5]
	s_waitcnt lgkmcnt(1)
	v_lshlrev_b32_e32 v154, 7, v153
	v_and_b32_e32 v154, 0x3f80, v154
	s_waitcnt lgkmcnt(0)
	v_and_b32_e32 v155, 0x7f, v156
	v_bitop3_b32 v155, v155, s9, v154 bitop3:0x36
	v_ashrrev_i32_e32 v154, 31, v156
	v_ashrrev_i32_e32 v157, 31, v153
	ds_bpermute_b32 v167, v148, v167
	s_nop 0
	v_and_b32_e32 v168, 0x7fffffff, v157
	v_bitop3_b32 v157, v154, v156, s98 bitop3:0x6c
	v_xor_b32_e32 v156, v168, v153
	v_pk_add_f32 v[156:157], v[156:157], v[156:157] op_sel:[1,0] op_sel_hi:[0,1]
	v_and_or_b32 v153, v156, s10, v141
	v_cndmask_b32_e64 v157, v238, v153, s[4:5]
	v_ashrrev_i32_e32 v153, 31, v187
	s_waitcnt lgkmcnt(0)
	v_ashrrev_i32_e32 v154, 31, v167
	s_nop 0
	s_nop 0
	v_bitop3_b32 v169, v153, v187, s98 bitop3:0x6c
	v_bitop3_b32 v168, v154, v167, s98 bitop3:0x6c
	v_pk_add_f32 v[168:169], v[168:169], v[168:169] op_sel:[1,0] op_sel_hi:[0,1]
	v_and_or_b32 v153, v168, s10, v141
	v_cndmask_b32_e64 v153, v238, v153, s[4:5]
	ds_write2st64_b32 v142, v165, v163 offset0:2 offset1:3
	ds_write2st64_b32 v142, v161, v159 offset0:4 offset1:5
	ds_write2st64_b32 v142, v157, v153 offset0:6 offset1:7
	s_waitcnt lgkmcnt(0)
	v_mov_b32_e32 v154, s84
	ds_read_b128 v[168:171], v154
	v_lshlrev_b32_e32 v156, 7, v167
	ds_read_b128 v[172:175], v154 offset:16
	ds_read_b128 v[176:179], v154 offset:32
	ds_read_b128 v[180:183], v154 offset:48
	v_and_b32_e32 v156, 0x3f80, v156
	s_waitcnt lgkmcnt(3)
	v_cmp_gt_f32_e64 s[16:17], v169, v185
	v_cmp_gt_f32_e32 vcc, v168, v185
	v_cmp_gt_f32_e64 s[98:99], v170, v185
	v_cndmask_b32_e64 v167, 0, 1, s[16:17]
	v_addc_co_u32_e32 v167, vcc, 0, v167, vcc
	v_cmp_gt_f32_e32 vcc, v171, v185
	v_cndmask_b32_e64 v168, 0, 1, s[98:99]
	s_nop 0
	v_addc_co_u32_e32 v167, vcc, v167, v168, vcc
	s_waitcnt lgkmcnt(2)
	v_cmp_gt_f32_e64 s[16:17], v172, v185
	v_cmp_gt_f32_e32 vcc, v173, v185
	v_cmp_gt_f32_e64 s[98:99], v174, v185
	v_cndmask_b32_e64 v168, 0, 1, s[16:17]
	v_addc_co_u32_e32 v167, vcc, v167, v168, vcc
	v_cmp_gt_f32_e32 vcc, v175, v185
	v_cndmask_b32_e64 v168, 0, 1, s[98:99]
	s_nop 0
	v_addc_co_u32_e32 v167, vcc, v167, v168, vcc
	s_waitcnt lgkmcnt(1)
	v_cmp_gt_f32_e64 s[16:17], v176, v185
	v_cmp_gt_f32_e32 vcc, v177, v185
	v_cmp_gt_f32_e64 s[98:99], v178, v185
	v_cndmask_b32_e64 v168, 0, 1, s[16:17]
	v_addc_co_u32_e32 v167, vcc, v167, v168, vcc
	v_cmp_gt_f32_e32 vcc, v179, v185
	v_cndmask_b32_e64 v168, 0, 1, s[98:99]
	s_nop 0
	v_addc_co_u32_e32 v167, vcc, v167, v168, vcc
	s_waitcnt lgkmcnt(0)
	v_cmp_gt_f32_e64 s[16:17], v180, v185
	v_cmp_gt_f32_e32 vcc, v181, v185
	s_nop 0
	v_cndmask_b32_e64 v168, 0, 1, s[16:17]
	v_addc_co_u32_e32 v167, vcc, v167, v168, vcc
	ds_read_b128 v[168:171], v154 offset:64
	v_cmp_gt_f32_e64 s[16:17], v182, v185
	v_cmp_gt_f32_e32 vcc, v183, v185
	s_nop 0
	v_cndmask_b32_e64 v172, 0, 1, s[16:17]
	v_addc_co_u32_e32 v167, vcc, v167, v172, vcc
	ds_read_b128 v[172:175], v154 offset:80
	s_waitcnt lgkmcnt(1)
	v_cmp_gt_f32_e64 s[16:17], v168, v185
	v_cmp_gt_f32_e32 vcc, v169, v185
	v_cmp_gt_f32_e64 s[98:99], v170, v185
	v_cndmask_b32_e64 v168, 0, 1, s[16:17]
	v_addc_co_u32_e32 v167, vcc, v167, v168, vcc
	v_cmp_gt_f32_e32 vcc, v171, v185
	v_cndmask_b32_e64 v168, 0, 1, s[98:99]
	s_nop 0
	v_addc_co_u32_e32 v167, vcc, v167, v168, vcc
	s_waitcnt lgkmcnt(0)
	v_cmp_gt_f32_e64 s[16:17], v172, v185
	v_cmp_gt_f32_e32 vcc, v173, v185
	s_nop 0
	v_cndmask_b32_e64 v168, 0, 1, s[16:17]
	v_addc_co_u32_e32 v167, vcc, v167, v168, vcc
	ds_read_b128 v[168:171], v154 offset:96
	v_cmp_gt_f32_e64 s[16:17], v174, v185
	v_cmp_gt_f32_e32 vcc, v175, v185
	s_nop 0
	v_cndmask_b32_e64 v172, 0, 1, s[16:17]
	v_addc_co_u32_e32 v167, vcc, v167, v172, vcc
	ds_read_b128 v[172:175], v154 offset:112
	s_waitcnt lgkmcnt(1)
	v_cmp_gt_f32_e64 s[16:17], v168, v185
	v_cmp_gt_f32_e32 vcc, v169, v185
	v_cmp_gt_f32_e64 s[98:99], v170, v185
	v_cndmask_b32_e64 v168, 0, 1, s[16:17]
	v_addc_co_u32_e32 v167, vcc, v167, v168, vcc
	v_cmp_gt_f32_e32 vcc, v171, v185
	v_cndmask_b32_e64 v168, 0, 1, s[98:99]
	s_nop 0
	v_addc_co_u32_e32 v167, vcc, v167, v168, vcc
	s_waitcnt lgkmcnt(0)
	v_cmp_gt_f32_e64 s[16:17], v172, v185
	v_cmp_gt_f32_e32 vcc, v173, v185
	s_nop 0
	v_cndmask_b32_e64 v168, 0, 1, s[16:17]
	v_addc_co_u32_e32 v167, vcc, v167, v168, vcc
	ds_read_b128 v[168:171], v154 offset:128
	v_cmp_gt_f32_e64 s[16:17], v174, v185
	v_cmp_gt_f32_e32 vcc, v175, v185
	s_nop 0
	v_cndmask_b32_e64 v172, 0, 1, s[16:17]
	v_addc_co_u32_e32 v167, vcc, v167, v172, vcc
	ds_read_b128 v[172:175], v154 offset:144
	s_waitcnt lgkmcnt(1)
	v_cmp_gt_f32_e64 s[16:17], v168, v185
	v_cmp_gt_f32_e32 vcc, v169, v185
	v_cmp_gt_f32_e64 s[98:99], v170, v185
	v_cndmask_b32_e64 v168, 0, 1, s[16:17]
	v_addc_co_u32_e32 v167, vcc, v167, v168, vcc
	v_cmp_gt_f32_e32 vcc, v171, v185
	v_cndmask_b32_e64 v168, 0, 1, s[98:99]
	s_nop 0
	v_addc_co_u32_e32 v167, vcc, v167, v168, vcc
	s_waitcnt lgkmcnt(0)
	v_cmp_gt_f32_e64 s[16:17], v172, v185
	v_cmp_gt_f32_e32 vcc, v173, v185
	s_nop 0
	v_cndmask_b32_e64 v168, 0, 1, s[16:17]
	v_addc_co_u32_e32 v167, vcc, v167, v168, vcc
	ds_read_b128 v[168:171], v154 offset:160
	v_cmp_gt_f32_e64 s[16:17], v174, v185
	v_cmp_gt_f32_e32 vcc, v175, v185
	s_nop 0
	v_cndmask_b32_e64 v172, 0, 1, s[16:17]
	v_addc_co_u32_e32 v167, vcc, v167, v172, vcc
	ds_read_b128 v[172:175], v154 offset:176
	s_waitcnt lgkmcnt(1)
	v_cmp_gt_f32_e64 s[16:17], v168, v185
	v_cmp_gt_f32_e32 vcc, v169, v185
	v_cmp_gt_f32_e64 s[98:99], v170, v185
	v_cndmask_b32_e64 v168, 0, 1, s[16:17]
	v_addc_co_u32_e32 v167, vcc, v167, v168, vcc
	v_cmp_gt_f32_e32 vcc, v171, v185
	v_cndmask_b32_e64 v168, 0, 1, s[98:99]
	s_nop 0
	v_addc_co_u32_e32 v167, vcc, v167, v168, vcc
	s_waitcnt lgkmcnt(0)
	v_cmp_gt_f32_e64 s[16:17], v172, v185
	v_cmp_gt_f32_e32 vcc, v173, v185
	s_nop 0
	v_cndmask_b32_e64 v168, 0, 1, s[16:17]
	v_addc_co_u32_e32 v167, vcc, v167, v168, vcc
	ds_read_b128 v[168:171], v154 offset:192
	v_cmp_gt_f32_e64 s[16:17], v174, v185
	v_cmp_gt_f32_e32 vcc, v175, v185
	s_nop 0
	v_cndmask_b32_e64 v172, 0, 1, s[16:17]
	v_addc_co_u32_e32 v167, vcc, v167, v172, vcc
	ds_read_b128 v[172:175], v154 offset:256
	s_waitcnt lgkmcnt(1)
	v_cmp_gt_f32_e32 vcc, v168, v185
	s_nop 1
	v_cndmask_b32_e64 v168, 0, 1, vcc
	v_cmp_gt_f32_e32 vcc, v169, v185
	v_and_b32_e32 v169, 0x7f, v187
	v_bitop3_b32 v156, v169, s9, v156 bitop3:0x36
	v_addc_co_u32_e32 v167, vcc, v167, v168, vcc
	s_nop 0
	s_nop 0
	s_nop 0
	s_nop 0
	s_nop 0
	v_cmp_gt_u32_e32 vcc, 16, v167
	s_and_b64 vcc, s[4:5], vcc
	s_nop 0
	v_cndmask_b32_e32 v167, v150, v167, vcc
	v_lshlrev_b32_e32 v167, 2, v167
	ds_permute_b32 v168, v167, v185
	s_waitcnt lgkmcnt(1)
	v_cmp_gt_f32_e32 vcc, v173, v186
	ds_permute_b32 v176, v167, v184
	s_waitcnt lgkmcnt(1)
	v_cndmask_b32_e64 v177, 0, v168, s[44:45]
	v_cndmask_b32_e64 v167, 0, 1, vcc
	v_cmp_gt_f32_e32 vcc, v172, v186
	ds_read_b128 v[168:171], v154 offset:272
	s_nop 0
	v_addc_co_u32_e32 v167, vcc, 0, v167, vcc
	v_cmp_gt_f32_e64 s[16:17], v174, v186
	v_cmp_gt_f32_e32 vcc, v175, v186
	s_nop 0
	v_cndmask_b32_e64 v172, 0, 1, s[16:17]
	v_addc_co_u32_e32 v167, vcc, v167, v172, vcc
	ds_read_b128 v[172:175], v154 offset:288
	s_waitcnt lgkmcnt(1)
	v_cmp_gt_f32_e64 s[16:17], v168, v186
	v_cmp_gt_f32_e32 vcc, v169, v186
	v_cmp_gt_f32_e64 s[98:99], v170, v186
	v_cndmask_b32_e64 v168, 0, 1, s[16:17]
	v_addc_co_u32_e32 v167, vcc, v167, v168, vcc
	v_cmp_gt_f32_e32 vcc, v171, v186
	v_cndmask_b32_e64 v168, 0, 1, s[98:99]
	s_nop 0
	v_addc_co_u32_e32 v167, vcc, v167, v168, vcc
	s_waitcnt lgkmcnt(0)
	v_cmp_gt_f32_e64 s[16:17], v172, v186
	v_cmp_gt_f32_e32 vcc, v173, v186
	s_nop 0
	v_cndmask_b32_e64 v168, 0, 1, s[16:17]
	v_addc_co_u32_e32 v167, vcc, v167, v168, vcc
	ds_read_b128 v[168:171], v154 offset:304
	v_cmp_gt_f32_e64 s[16:17], v174, v186
	v_cmp_gt_f32_e32 vcc, v175, v186
	s_nop 0
	v_cndmask_b32_e64 v172, 0, 1, s[16:17]
	v_addc_co_u32_e32 v167, vcc, v167, v172, vcc
	ds_read_b128 v[172:175], v154 offset:320
	s_waitcnt lgkmcnt(1)
	v_cmp_gt_f32_e64 s[16:17], v168, v186
	v_cmp_gt_f32_e32 vcc, v169, v186
	v_cmp_gt_f32_e64 s[98:99], v170, v186
	v_cndmask_b32_e64 v168, 0, 1, s[16:17]
	v_addc_co_u32_e32 v167, vcc, v167, v168, vcc
	v_cmp_gt_f32_e32 vcc, v171, v186
	v_cndmask_b32_e64 v168, 0, 1, s[98:99]
	s_nop 0
	v_addc_co_u32_e32 v167, vcc, v167, v168, vcc
	s_waitcnt lgkmcnt(0)
	v_cmp_gt_f32_e64 s[16:17], v172, v186
	v_cmp_gt_f32_e32 vcc, v173, v186
	s_nop 0
	v_cndmask_b32_e64 v168, 0, 1, s[16:17]
	v_addc_co_u32_e32 v167, vcc, v167, v168, vcc
	ds_read_b128 v[168:171], v154 offset:336
	v_cmp_gt_f32_e64 s[16:17], v174, v186
	v_cmp_gt_f32_e32 vcc, v175, v186
	s_nop 0
	v_cndmask_b32_e64 v172, 0, 1, s[16:17]
	v_addc_co_u32_e32 v167, vcc, v167, v172, vcc
	ds_read_b128 v[172:175], v154 offset:352
	s_waitcnt lgkmcnt(1)
	v_cmp_gt_f32_e64 s[16:17], v168, v186
	v_cmp_gt_f32_e32 vcc, v169, v186
	v_cmp_gt_f32_e64 s[98:99], v170, v186
	v_cndmask_b32_e64 v168, 0, 1, s[16:17]
	v_addc_co_u32_e32 v167, vcc, v167, v168, vcc
	v_cmp_gt_f32_e32 vcc, v171, v186
	v_cndmask_b32_e64 v168, 0, 1, s[98:99]
	s_nop 0
	v_addc_co_u32_e32 v167, vcc, v167, v168, vcc
	s_waitcnt lgkmcnt(0)
	v_cmp_gt_f32_e64 s[16:17], v172, v186
	v_cmp_gt_f32_e32 vcc, v173, v186
	s_nop 0
	v_cndmask_b32_e64 v168, 0, 1, s[16:17]
	v_addc_co_u32_e32 v167, vcc, v167, v168, vcc
	ds_read_b128 v[168:171], v154 offset:368
	v_cmp_gt_f32_e64 s[16:17], v174, v186
	v_cmp_gt_f32_e32 vcc, v175, v186
	s_nop 0
	v_cndmask_b32_e64 v172, 0, 1, s[16:17]
	v_addc_co_u32_e32 v167, vcc, v167, v172, vcc
	ds_read_b128 v[172:175], v154 offset:384
	s_waitcnt lgkmcnt(1)
	v_cmp_gt_f32_e64 s[16:17], v168, v186
	v_cmp_gt_f32_e32 vcc, v169, v186
	v_cmp_gt_f32_e64 s[98:99], v170, v186
	v_cndmask_b32_e64 v168, 0, 1, s[16:17]
	v_addc_co_u32_e32 v167, vcc, v167, v168, vcc
	v_cmp_gt_f32_e32 vcc, v171, v186
	v_cndmask_b32_e64 v168, 0, 1, s[98:99]
	s_nop 0
	v_addc_co_u32_e32 v167, vcc, v167, v168, vcc
	s_waitcnt lgkmcnt(0)
	v_cmp_gt_f32_e64 s[16:17], v172, v186
	v_cmp_gt_f32_e32 vcc, v173, v186
	s_nop 0
	v_cndmask_b32_e64 v168, 0, 1, s[16:17]
	v_addc_co_u32_e32 v167, vcc, v167, v168, vcc
	ds_read_b128 v[168:171], v154 offset:400
	v_cmp_gt_f32_e64 s[16:17], v174, v186
	v_cmp_gt_f32_e32 vcc, v175, v186
	s_nop 0
	v_cndmask_b32_e64 v172, 0, 1, s[16:17]
	v_addc_co_u32_e32 v167, vcc, v167, v172, vcc
	ds_read_b128 v[172:175], v154 offset:416
	s_waitcnt lgkmcnt(1)
	v_cmp_gt_f32_e64 s[16:17], v168, v186
	v_cmp_gt_f32_e32 vcc, v169, v186
	v_cmp_gt_f32_e64 s[98:99], v170, v186
	v_cndmask_b32_e64 v168, 0, 1, s[16:17]
	v_addc_co_u32_e32 v167, vcc, v167, v168, vcc
	v_cmp_gt_f32_e32 vcc, v171, v186
	v_cndmask_b32_e64 v168, 0, 1, s[98:99]
	s_nop 0
	v_addc_co_u32_e32 v167, vcc, v167, v168, vcc
	s_waitcnt lgkmcnt(0)
	v_cmp_gt_f32_e64 s[16:17], v172, v186
	v_cmp_gt_f32_e32 vcc, v173, v186
	s_nop 0
	v_cndmask_b32_e64 v168, 0, 1, s[16:17]
	v_addc_co_u32_e32 v167, vcc, v167, v168, vcc
	ds_read_b128 v[168:171], v154 offset:432
	v_cmp_gt_f32_e64 s[16:17], v174, v186
	v_cmp_gt_f32_e32 vcc, v175, v186
	s_nop 0
	v_cndmask_b32_e64 v172, 0, 1, s[16:17]
	v_addc_co_u32_e32 v167, vcc, v167, v172, vcc
	ds_read_b128 v[172:175], v154 offset:448
	s_waitcnt lgkmcnt(1)
	v_cmp_gt_f32_e64 s[16:17], v168, v186
	v_cmp_gt_f32_e32 vcc, v169, v186
	v_cmp_gt_f32_e64 s[98:99], v170, v186
	v_cndmask_b32_e64 v168, 0, 1, s[16:17]
	v_addc_co_u32_e32 v167, vcc, v167, v168, vcc
	v_cmp_gt_f32_e32 vcc, v171, v186
	v_cndmask_b32_e64 v168, 0, 1, s[98:99]
	s_nop 0
	v_addc_co_u32_e32 v167, vcc, v167, v168, vcc
	s_waitcnt lgkmcnt(0)
	v_cmp_gt_f32_e64 s[16:17], v172, v186
	v_cmp_gt_f32_e32 vcc, v173, v186
	s_nop 0
	v_cndmask_b32_e64 v168, 0, 1, s[16:17]
	v_addc_co_u32_e32 v167, vcc, v167, v168, vcc
	s_nop 0
	s_nop 1
	s_nop 0
	s_nop 0
	ds_read_b128 v[172:175], v154 offset:528
	s_nop 0
	s_nop 0
	ds_read_b128 v[168:171], v154 offset:512
	v_cmp_gt_u32_e32 vcc, 16, v167
	v_add_u32_e32 v167, 16, v167
	s_and_b64 vcc, s[4:5], vcc
	v_cndmask_b32_e32 v167, v151, v167, vcc
	v_lshlrev_b32_e32 v167, 2, v167
	s_waitcnt lgkmcnt(0)
	v_cmp_gt_f32_e32 vcc, v169, v165
	ds_permute_b32 v179, v167, v166
	ds_permute_b32 v178, v167, v186
	v_cndmask_b32_e64 v166, 0, 1, vcc
	v_cmp_gt_f32_e32 vcc, v168, v165
	s_nop 1
	v_addc_co_u32_e32 v166, vcc, 0, v166, vcc
	v_cmp_gt_f32_e64 s[16:17], v170, v165
	v_cmp_gt_f32_e32 vcc, v171, v165
	v_cmp_gt_f32_e64 s[98:99], v172, v165
	v_cndmask_b32_e64 v167, 0, 1, s[16:17]
	v_addc_co_u32_e32 v166, vcc, v166, v167, vcc
	v_cmp_gt_f32_e32 vcc, v173, v165
	v_cndmask_b32_e64 v167, 0, 1, s[98:99]
	s_nop 0
	v_addc_co_u32_e32 v170, vcc, v166, v167, vcc
	ds_read_b128 v[166:169], v154 offset:544
	v_cmp_gt_f32_e64 s[16:17], v174, v165
	v_cmp_gt_f32_e32 vcc, v175, v165
	s_nop 0
	v_cndmask_b32_e64 v171, 0, 1, s[16:17]
	v_addc_co_u32_e32 v174, vcc, v170, v171, vcc
	ds_read_b128 v[170:173], v154 offset:560
	s_waitcnt lgkmcnt(1)
	v_cmp_gt_f32_e64 s[16:17], v166, v165
	v_cmp_gt_f32_e32 vcc, v167, v165
	v_cmp_gt_f32_e64 s[98:99], v168, v165
	v_cndmask_b32_e64 v166, 0, 1, s[16:17]
	v_addc_co_u32_e32 v166, vcc, v174, v166, vcc
	v_cmp_gt_f32_e32 vcc, v169, v165
	v_cndmask_b32_e64 v167, 0, 1, s[98:99]
	s_nop 0
	v_addc_co_u32_e32 v166, vcc, v166, v167, vcc
	s_waitcnt lgkmcnt(0)
	v_cmp_gt_f32_e64 s[16:17], v170, v165
	v_cmp_gt_f32_e32 vcc, v171, v165
	s_nop 0
	v_cndmask_b32_e64 v167, 0, 1, s[16:17]
	v_addc_co_u32_e32 v170, vcc, v166, v167, vcc
	ds_read_b128 v[166:169], v154 offset:576
	v_cmp_gt_f32_e64 s[16:17], v172, v165
	v_cmp_gt_f32_e32 vcc, v173, v165
	s_nop 0
	v_cndmask_b32_e64 v171, 0, 1, s[16:17]
	v_addc_co_u32_e32 v174, vcc, v170, v171, vcc
	ds_read_b128 v[170:173], v154 offset:592
	s_waitcnt lgkmcnt(1)
	v_cmp_gt_f32_e64 s[16:17], v166, v165
	v_cmp_gt_f32_e32 vcc, v167, v165
	v_cmp_gt_f32_e64 s[98:99], v168, v165
	v_cndmask_b32_e64 v166, 0, 1, s[16:17]
	v_addc_co_u32_e32 v166, vcc, v174, v166, vcc
	v_cmp_gt_f32_e32 vcc, v169, v165
	v_cndmask_b32_e64 v167, 0, 1, s[98:99]
	s_nop 0
	v_addc_co_u32_e32 v166, vcc, v166, v167, vcc
	s_waitcnt lgkmcnt(0)
	v_cmp_gt_f32_e64 s[16:17], v170, v165
	v_cmp_gt_f32_e32 vcc, v171, v165
	s_nop 0
	v_cndmask_b32_e64 v167, 0, 1, s[16:17]
	v_addc_co_u32_e32 v170, vcc, v166, v167, vcc
	ds_read_b128 v[166:169], v154 offset:608
	v_cmp_gt_f32_e64 s[16:17], v172, v165
	v_cmp_gt_f32_e32 vcc, v173, v165
	s_nop 0
	v_cndmask_b32_e64 v171, 0, 1, s[16:17]
	v_addc_co_u32_e32 v174, vcc, v170, v171, vcc
	ds_read_b128 v[170:173], v154 offset:624
	s_waitcnt lgkmcnt(1)
	v_cmp_gt_f32_e64 s[16:17], v166, v165
	v_cmp_gt_f32_e32 vcc, v167, v165
	v_cmp_gt_f32_e64 s[98:99], v168, v165
	v_cndmask_b32_e64 v166, 0, 1, s[16:17]
	v_addc_co_u32_e32 v166, vcc, v174, v166, vcc
	v_cmp_gt_f32_e32 vcc, v169, v165
	v_cndmask_b32_e64 v167, 0, 1, s[98:99]
	s_nop 0
	v_addc_co_u32_e32 v166, vcc, v166, v167, vcc
	s_waitcnt lgkmcnt(0)
	v_cmp_gt_f32_e64 s[16:17], v170, v165
	v_cmp_gt_f32_e32 vcc, v171, v165
	s_nop 0
	v_cndmask_b32_e64 v167, 0, 1, s[16:17]
	v_addc_co_u32_e32 v170, vcc, v166, v167, vcc
	ds_read_b128 v[166:169], v154 offset:640
	v_cmp_gt_f32_e64 s[16:17], v172, v165
	v_cmp_gt_f32_e32 vcc, v173, v165
	s_nop 0
	v_cndmask_b32_e64 v171, 0, 1, s[16:17]
	v_addc_co_u32_e32 v174, vcc, v170, v171, vcc
	ds_read_b128 v[170:173], v154 offset:656
	s_waitcnt lgkmcnt(1)
	v_cmp_gt_f32_e64 s[16:17], v166, v165
	v_cmp_gt_f32_e32 vcc, v167, v165
	v_cmp_gt_f32_e64 s[98:99], v168, v165
	v_cndmask_b32_e64 v166, 0, 1, s[16:17]
	v_addc_co_u32_e32 v166, vcc, v174, v166, vcc
	v_cmp_gt_f32_e32 vcc, v169, v165
	v_cndmask_b32_e64 v167, 0, 1, s[98:99]
	s_nop 0
	v_addc_co_u32_e32 v166, vcc, v166, v167, vcc
	s_waitcnt lgkmcnt(0)
	v_cmp_gt_f32_e64 s[16:17], v170, v165
	v_cmp_gt_f32_e32 vcc, v171, v165
	s_nop 0
	v_cndmask_b32_e64 v167, 0, 1, s[16:17]
	v_addc_co_u32_e32 v170, vcc, v166, v167, vcc
	ds_read_b128 v[166:169], v154 offset:672
	v_cmp_gt_f32_e64 s[16:17], v172, v165
	v_cmp_gt_f32_e32 vcc, v173, v165
	s_nop 0
	v_cndmask_b32_e64 v171, 0, 1, s[16:17]
	v_addc_co_u32_e32 v174, vcc, v170, v171, vcc
	ds_read_b128 v[170:173], v154 offset:688
	s_waitcnt lgkmcnt(1)
	v_cmp_gt_f32_e64 s[16:17], v166, v165
	v_cmp_gt_f32_e32 vcc, v167, v165
	v_cmp_gt_f32_e64 s[98:99], v168, v165
	v_cndmask_b32_e64 v166, 0, 1, s[16:17]
	v_addc_co_u32_e32 v166, vcc, v174, v166, vcc
	v_cmp_gt_f32_e32 vcc, v169, v165
	v_cndmask_b32_e64 v167, 0, 1, s[98:99]
	s_nop 0
	v_addc_co_u32_e32 v166, vcc, v166, v167, vcc
	s_waitcnt lgkmcnt(0)
	v_cmp_gt_f32_e64 s[16:17], v170, v165
	v_cmp_gt_f32_e32 vcc, v171, v165
	s_nop 0
	v_cndmask_b32_e64 v167, 0, 1, s[16:17]
	v_addc_co_u32_e32 v170, vcc, v166, v167, vcc
	ds_read_b128 v[166:169], v154 offset:704
	v_cmp_gt_f32_e64 s[16:17], v172, v165
	v_cmp_gt_f32_e32 vcc, v173, v165
	s_nop 0
	v_cndmask_b32_e64 v171, 0, 1, s[16:17]
	v_addc_co_u32_e32 v174, vcc, v170, v171, vcc
	ds_read_b128 v[170:173], v154 offset:768
	s_waitcnt lgkmcnt(1)
	v_cmp_gt_f32_e64 s[16:17], v166, v165
	v_cmp_gt_f32_e32 vcc, v167, v165
	s_nop 0
	v_cndmask_b32_e64 v166, 0, 1, s[16:17]
	v_addc_co_u32_e32 v166, vcc, v174, v166, vcc
	s_nop 0
	v_cndmask_b32_e64 v168, v177, v178, s[46:47]
	s_nop 0
	s_nop 0
	s_nop 0
	s_nop 1
	s_nop 0
	v_cmp_gt_u32_e32 vcc, 16, v166
	v_add_u32_e32 v166, 32, v166
	s_and_b64 vcc, s[4:5], vcc
	v_cndmask_b32_e32 v166, v152, v166, vcc
	v_lshlrev_b32_e32 v166, 2, v166
	ds_permute_b32 v165, v166, v165
	s_waitcnt lgkmcnt(1)
	v_cmp_gt_f32_e32 vcc, v171, v163
	v_cndmask_b32_e64 v167, 0, v176, s[44:45]
	ds_permute_b32 v175, v166, v164
	v_cndmask_b32_e64 v164, 0, 1, vcc
	v_cmp_gt_f32_e32 vcc, v170, v163
	v_cndmask_b32_e64 v174, v167, v179, s[46:47]
	s_waitcnt lgkmcnt(1)
	v_cndmask_b32_e64 v176, v168, v165, s[48:49]
	v_addc_co_u32_e32 v168, vcc, 0, v164, vcc
	ds_read_b128 v[164:167], v154 offset:784
	v_cmp_gt_f32_e64 s[16:17], v172, v163
	v_cmp_gt_f32_e32 vcc, v173, v163
	s_nop 0
	v_cndmask_b32_e64 v169, 0, 1, s[16:17]
	v_addc_co_u32_e32 v172, vcc, v168, v169, vcc
	ds_read_b128 v[168:171], v154 offset:800
	s_waitcnt lgkmcnt(1)
	v_cmp_gt_f32_e64 s[16:17], v164, v163
	v_cmp_gt_f32_e32 vcc, v165, v163
	v_cmp_gt_f32_e64 s[98:99], v166, v163
	v_cndmask_b32_e64 v164, 0, 1, s[16:17]
	v_addc_co_u32_e32 v164, vcc, v172, v164, vcc
	v_cmp_gt_f32_e32 vcc, v167, v163
	v_cndmask_b32_e64 v165, 0, 1, s[98:99]
	s_nop 0
	v_addc_co_u32_e32 v164, vcc, v164, v165, vcc
	s_waitcnt lgkmcnt(0)
	v_cmp_gt_f32_e64 s[16:17], v168, v163
	v_cmp_gt_f32_e32 vcc, v169, v163
	s_nop 0
	v_cndmask_b32_e64 v165, 0, 1, s[16:17]
	v_addc_co_u32_e32 v168, vcc, v164, v165, vcc
	ds_read_b128 v[164:167], v154 offset:816
	v_cmp_gt_f32_e64 s[16:17], v170, v163
	v_cmp_gt_f32_e32 vcc, v171, v163
	s_nop 0
	v_cndmask_b32_e64 v169, 0, 1, s[16:17]
	v_addc_co_u32_e32 v172, vcc, v168, v169, vcc
	ds_read_b128 v[168:171], v154 offset:832
	s_waitcnt lgkmcnt(1)
	v_cmp_gt_f32_e64 s[16:17], v164, v163
	v_cmp_gt_f32_e32 vcc, v165, v163
	v_cmp_gt_f32_e64 s[98:99], v166, v163
	v_cndmask_b32_e64 v164, 0, 1, s[16:17]
	v_addc_co_u32_e32 v164, vcc, v172, v164, vcc
	v_cmp_gt_f32_e32 vcc, v167, v163
	v_cndmask_b32_e64 v165, 0, 1, s[98:99]
	s_nop 0
	v_addc_co_u32_e32 v164, vcc, v164, v165, vcc
	s_waitcnt lgkmcnt(0)
	v_cmp_gt_f32_e64 s[16:17], v168, v163
	v_cmp_gt_f32_e32 vcc, v169, v163
	s_nop 0
	v_cndmask_b32_e64 v165, 0, 1, s[16:17]
	v_addc_co_u32_e32 v168, vcc, v164, v165, vcc
	ds_read_b128 v[164:167], v154 offset:848
	v_cmp_gt_f32_e64 s[16:17], v170, v163
	v_cmp_gt_f32_e32 vcc, v171, v163
	s_nop 0
	v_cndmask_b32_e64 v169, 0, 1, s[16:17]
	v_addc_co_u32_e32 v172, vcc, v168, v169, vcc
	ds_read_b128 v[168:171], v154 offset:864
	s_waitcnt lgkmcnt(1)
	v_cmp_gt_f32_e64 s[16:17], v164, v163
	v_cmp_gt_f32_e32 vcc, v165, v163
	v_cmp_gt_f32_e64 s[98:99], v166, v163
	v_cndmask_b32_e64 v164, 0, 1, s[16:17]
	v_addc_co_u32_e32 v164, vcc, v172, v164, vcc
	v_cmp_gt_f32_e32 vcc, v167, v163
	v_cndmask_b32_e64 v165, 0, 1, s[98:99]
	s_nop 0
	v_addc_co_u32_e32 v164, vcc, v164, v165, vcc
	s_waitcnt lgkmcnt(0)
	v_cmp_gt_f32_e64 s[16:17], v168, v163
	v_cmp_gt_f32_e32 vcc, v169, v163
	s_nop 0
	v_cndmask_b32_e64 v165, 0, 1, s[16:17]
	v_addc_co_u32_e32 v168, vcc, v164, v165, vcc
	ds_read_b128 v[164:167], v154 offset:880
	v_cmp_gt_f32_e64 s[16:17], v170, v163
	v_cmp_gt_f32_e32 vcc, v171, v163
	s_nop 0
	v_cndmask_b32_e64 v169, 0, 1, s[16:17]
	v_addc_co_u32_e32 v172, vcc, v168, v169, vcc
	ds_read_b128 v[168:171], v154 offset:896
	s_waitcnt lgkmcnt(1)
	v_cmp_gt_f32_e64 s[16:17], v164, v163
	v_cmp_gt_f32_e32 vcc, v165, v163
	v_cmp_gt_f32_e64 s[98:99], v166, v163
	v_cndmask_b32_e64 v164, 0, 1, s[16:17]
	v_addc_co_u32_e32 v164, vcc, v172, v164, vcc
	v_cmp_gt_f32_e32 vcc, v167, v163
	v_cndmask_b32_e64 v165, 0, 1, s[98:99]
	s_nop 0
	v_addc_co_u32_e32 v164, vcc, v164, v165, vcc
	s_waitcnt lgkmcnt(0)
	v_cmp_gt_f32_e64 s[16:17], v168, v163
	v_cmp_gt_f32_e32 vcc, v169, v163
	s_nop 0
	v_cndmask_b32_e64 v165, 0, 1, s[16:17]
	v_addc_co_u32_e32 v168, vcc, v164, v165, vcc
	ds_read_b128 v[164:167], v154 offset:912
	v_cmp_gt_f32_e64 s[16:17], v170, v163
	v_cmp_gt_f32_e32 vcc, v171, v163
	s_nop 0
	v_cndmask_b32_e64 v169, 0, 1, s[16:17]
	v_addc_co_u32_e32 v172, vcc, v168, v169, vcc
	ds_read_b128 v[168:171], v154 offset:928
	s_waitcnt lgkmcnt(1)
	v_cmp_gt_f32_e64 s[16:17], v164, v163
	v_cmp_gt_f32_e32 vcc, v165, v163
	v_cmp_gt_f32_e64 s[98:99], v166, v163
	v_cndmask_b32_e64 v164, 0, 1, s[16:17]
	v_addc_co_u32_e32 v164, vcc, v172, v164, vcc
	v_cmp_gt_f32_e32 vcc, v167, v163
	v_cndmask_b32_e64 v165, 0, 1, s[98:99]
	s_nop 0
	v_addc_co_u32_e32 v164, vcc, v164, v165, vcc
	s_waitcnt lgkmcnt(0)
	v_cmp_gt_f32_e64 s[16:17], v168, v163
	v_cmp_gt_f32_e32 vcc, v169, v163
	s_nop 0
	v_cndmask_b32_e64 v165, 0, 1, s[16:17]
	v_addc_co_u32_e32 v168, vcc, v164, v165, vcc
	ds_read_b128 v[164:167], v154 offset:944
	v_cmp_gt_f32_e64 s[16:17], v170, v163
	v_cmp_gt_f32_e32 vcc, v171, v163
	s_nop 0
	v_cndmask_b32_e64 v169, 0, 1, s[16:17]
	v_addc_co_u32_e32 v172, vcc, v168, v169, vcc
	ds_read_b128 v[168:171], v154 offset:960
	s_waitcnt lgkmcnt(1)
	v_cmp_gt_f32_e64 s[16:17], v164, v163
	v_cmp_gt_f32_e32 vcc, v165, v163
	v_cmp_gt_f32_e64 s[98:99], v166, v163
	v_cndmask_b32_e64 v164, 0, 1, s[16:17]
	v_addc_co_u32_e32 v164, vcc, v172, v164, vcc
	v_cmp_gt_f32_e32 vcc, v167, v163
	v_cndmask_b32_e64 v165, 0, 1, s[98:99]
	s_nop 0
	v_addc_co_u32_e32 v164, vcc, v164, v165, vcc
	s_waitcnt lgkmcnt(0)
	v_cmp_gt_f32_e64 s[16:17], v168, v163
	v_cmp_gt_f32_e32 vcc, v169, v163
	s_nop 0
	v_cndmask_b32_e64 v165, 0, 1, s[16:17]
	v_addc_co_u32_e32 v164, vcc, v164, v165, vcc
	s_nop 0
	s_nop 0
	s_nop 0
	s_nop 0
	v_cmp_gt_u32_e32 vcc, 16, v164
	v_add_u32_e32 v164, 48, v164
	s_and_b64 vcc, s[4:5], vcc
	v_cndmask_b32_e32 v168, v140, v164, vcc
	ds_read_b128 v[164:167], v154 offset:1024
	v_lshlrev_b32_e32 v168, 2, v168
	ds_permute_b32 v172, v168, v163
	ds_permute_b32 v173, v168, v162
	ds_read_b128 v[168:171], v154 offset:1040
	s_waitcnt lgkmcnt(3)
	v_cmp_gt_f32_e64 s[16:17], v165, v161
	v_cmp_gt_f32_e32 vcc, v164, v161
	v_cmp_gt_f32_e64 s[98:99], v166, v161
	v_cndmask_b32_e64 v162, 0, 1, s[16:17]
	v_addc_co_u32_e32 v162, vcc, 0, v162, vcc
	v_cmp_gt_f32_e32 vcc, v167, v161
	v_cndmask_b32_e64 v163, 0, 1, s[98:99]
	s_nop 0
	v_addc_co_u32_e32 v162, vcc, v162, v163, vcc
	s_waitcnt lgkmcnt(0)
	v_cmp_gt_f32_e64 s[16:17], v168, v161
	v_cmp_gt_f32_e32 vcc, v169, v161
	s_nop 0
	v_cndmask_b32_e64 v163, 0, 1, s[16:17]
	v_addc_co_u32_e32 v166, vcc, v162, v163, vcc
	ds_read_b128 v[162:165], v154 offset:1056
	v_cmp_gt_f32_e64 s[16:17], v170, v161
	v_cmp_gt_f32_e32 vcc, v171, v161
	s_nop 0
	v_cndmask_b32_e64 v167, 0, 1, s[16:17]
	v_addc_co_u32_e32 v170, vcc, v166, v167, vcc
	ds_read_b128 v[166:169], v154 offset:1072
	s_waitcnt lgkmcnt(1)
	v_cmp_gt_f32_e64 s[16:17], v162, v161
	v_cmp_gt_f32_e32 vcc, v163, v161
	v_cmp_gt_f32_e64 s[98:99], v164, v161
	v_cndmask_b32_e64 v162, 0, 1, s[16:17]
	v_addc_co_u32_e32 v162, vcc, v170, v162, vcc
	v_cmp_gt_f32_e32 vcc, v165, v161
	v_cndmask_b32_e64 v163, 0, 1, s[98:99]
	s_nop 0
	v_addc_co_u32_e32 v162, vcc, v162, v163, vcc
	s_waitcnt lgkmcnt(0)
	v_cmp_gt_f32_e64 s[16:17], v166, v161
	v_cmp_gt_f32_e32 vcc, v167, v161
	s_nop 0
	v_cndmask_b32_e64 v163, 0, 1, s[16:17]
	v_addc_co_u32_e32 v166, vcc, v162, v163, vcc
	ds_read_b128 v[162:165], v154 offset:1088
	v_cmp_gt_f32_e64 s[16:17], v168, v161
	v_cmp_gt_f32_e32 vcc, v169, v161
	s_nop 0
	v_cndmask_b32_e64 v167, 0, 1, s[16:17]
	v_addc_co_u32_e32 v170, vcc, v166, v167, vcc
	ds_read_b128 v[166:169], v154 offset:1104
	s_waitcnt lgkmcnt(1)
	v_cmp_gt_f32_e64 s[16:17], v162, v161
	v_cmp_gt_f32_e32 vcc, v163, v161
	v_cmp_gt_f32_e64 s[98:99], v164, v161
	v_cndmask_b32_e64 v162, 0, 1, s[16:17]
	v_addc_co_u32_e32 v162, vcc, v170, v162, vcc
	v_cmp_gt_f32_e32 vcc, v165, v161
	v_cndmask_b32_e64 v163, 0, 1, s[98:99]
	s_nop 0
	v_addc_co_u32_e32 v162, vcc, v162, v163, vcc
	s_waitcnt lgkmcnt(0)
	v_cmp_gt_f32_e64 s[16:17], v166, v161
	v_cmp_gt_f32_e32 vcc, v167, v161
	s_nop 0
	v_cndmask_b32_e64 v163, 0, 1, s[16:17]
	v_addc_co_u32_e32 v166, vcc, v162, v163, vcc
	ds_read_b128 v[162:165], v154 offset:1120
	v_cmp_gt_f32_e64 s[16:17], v168, v161
	v_cmp_gt_f32_e32 vcc, v169, v161
	s_nop 0
	v_cndmask_b32_e64 v167, 0, 1, s[16:17]
	v_addc_co_u32_e32 v170, vcc, v166, v167, vcc
	ds_read_b128 v[166:169], v154 offset:1136
	s_waitcnt lgkmcnt(1)
	v_cmp_gt_f32_e64 s[16:17], v162, v161
	v_cmp_gt_f32_e32 vcc, v163, v161
	v_cmp_gt_f32_e64 s[98:99], v164, v161
	v_cndmask_b32_e64 v162, 0, 1, s[16:17]
	v_addc_co_u32_e32 v162, vcc, v170, v162, vcc
	v_cmp_gt_f32_e32 vcc, v165, v161
	v_cndmask_b32_e64 v163, 0, 1, s[98:99]
	s_nop 0
	v_addc_co_u32_e32 v162, vcc, v162, v163, vcc
	s_waitcnt lgkmcnt(0)
	v_cmp_gt_f32_e64 s[16:17], v166, v161
	v_cmp_gt_f32_e32 vcc, v167, v161
	s_nop 0
	v_cndmask_b32_e64 v163, 0, 1, s[16:17]
	v_addc_co_u32_e32 v166, vcc, v162, v163, vcc
	ds_read_b128 v[162:165], v154 offset:1152
	v_cmp_gt_f32_e64 s[16:17], v168, v161
	v_cmp_gt_f32_e32 vcc, v169, v161
	s_nop 0
	v_cndmask_b32_e64 v167, 0, 1, s[16:17]
	v_addc_co_u32_e32 v170, vcc, v166, v167, vcc
	ds_read_b128 v[166:169], v154 offset:1168
	s_waitcnt lgkmcnt(1)
	v_cmp_gt_f32_e64 s[16:17], v162, v161
	v_cmp_gt_f32_e32 vcc, v163, v161
	v_cmp_gt_f32_e64 s[98:99], v164, v161
	v_cndmask_b32_e64 v162, 0, 1, s[16:17]
	v_addc_co_u32_e32 v162, vcc, v170, v162, vcc
	v_cmp_gt_f32_e32 vcc, v165, v161
	v_cndmask_b32_e64 v163, 0, 1, s[98:99]
	s_nop 0
	v_addc_co_u32_e32 v162, vcc, v162, v163, vcc
	s_waitcnt lgkmcnt(0)
	v_cmp_gt_f32_e64 s[16:17], v166, v161
	v_cmp_gt_f32_e32 vcc, v167, v161
	s_nop 0
	v_cndmask_b32_e64 v163, 0, 1, s[16:17]
	v_addc_co_u32_e32 v166, vcc, v162, v163, vcc
	ds_read_b128 v[162:165], v154 offset:1184
	v_cmp_gt_f32_e64 s[16:17], v168, v161
	v_cmp_gt_f32_e32 vcc, v169, v161
	s_nop 0
	v_cndmask_b32_e64 v167, 0, 1, s[16:17]
	v_addc_co_u32_e32 v170, vcc, v166, v167, vcc
	ds_read_b128 v[166:169], v154 offset:1200
	s_waitcnt lgkmcnt(1)
	v_cmp_gt_f32_e64 s[16:17], v162, v161
	v_cmp_gt_f32_e32 vcc, v163, v161
	v_cmp_gt_f32_e64 s[98:99], v164, v161
	v_cndmask_b32_e64 v162, 0, 1, s[16:17]
	v_addc_co_u32_e32 v162, vcc, v170, v162, vcc
	v_cmp_gt_f32_e32 vcc, v165, v161
	v_cndmask_b32_e64 v163, 0, 1, s[98:99]
	s_nop 0
	v_addc_co_u32_e32 v162, vcc, v162, v163, vcc
	s_waitcnt lgkmcnt(0)
	v_cmp_gt_f32_e64 s[16:17], v166, v161
	v_cmp_gt_f32_e32 vcc, v167, v161
	s_nop 0
	v_cndmask_b32_e64 v163, 0, 1, s[16:17]
	v_addc_co_u32_e32 v166, vcc, v162, v163, vcc
	ds_read_b128 v[162:165], v154 offset:1216
	v_cmp_gt_f32_e64 s[16:17], v168, v161
	v_cmp_gt_f32_e32 vcc, v169, v161
	s_nop 0
	v_cndmask_b32_e64 v167, 0, 1, s[16:17]
	v_addc_co_u32_e32 v170, vcc, v166, v167, vcc
	ds_read_b128 v[166:169], v154 offset:1280
	s_waitcnt lgkmcnt(1)
	v_cmp_gt_f32_e64 s[16:17], v162, v161
	v_cmp_gt_f32_e32 vcc, v163, v161
	s_nop 0
	v_cndmask_b32_e64 v162, 0, 1, s[16:17]
	v_addc_co_u32_e32 v162, vcc, v170, v162, vcc
	s_nop 0
	s_nop 0
	s_nop 0
	s_nop 0
	v_cmp_gt_u32_e32 vcc, 16, v162
	s_and_b64 vcc, s[4:5], vcc
	s_nop 0
	v_cndmask_b32_e32 v162, v150, v162, vcc
	v_lshlrev_b32_e32 v163, 2, v162
	ds_permute_b32 v164, v163, v161
	s_waitcnt lgkmcnt(1)
	v_cmp_gt_f32_e32 vcc, v167, v159
	ds_permute_b32 v160, v163, v160
	v_cndmask_b32_e64 v162, v176, v172, s[50:51]
	v_cndmask_b32_e64 v161, v174, v175, s[48:49]
	s_waitcnt lgkmcnt(1)
	v_cndmask_b32_e64 v163, 0, v164, s[44:45]
	v_cndmask_b32_e64 v164, 0, 1, vcc
	v_cmp_gt_f32_e32 vcc, v166, v159
	s_waitcnt lgkmcnt(0)
	v_cndmask_b32_e64 v160, 0, v160, s[44:45]
	v_cndmask_b32_e64 v161, v161, v173, s[50:51]
	v_addc_co_u32_e32 v170, vcc, 0, v164, vcc
	ds_read_b128 v[164:167], v154 offset:1296
	v_cmp_gt_f32_e32 vcc, v168, v159
	v_lshlrev_b32_e32 v161, 7, v161
	s_nop 0
	v_cndmask_b32_e64 v168, 0, 1, vcc
	v_cmp_gt_f32_e32 vcc, v169, v159
	s_nop 1
	v_addc_co_u32_e32 v172, vcc, v170, v168, vcc
	ds_read_b128 v[168:171], v154 offset:1312
	s_waitcnt lgkmcnt(1)
	v_cmp_gt_f32_e64 s[16:17], v164, v159
	v_cmp_gt_f32_e32 vcc, v165, v159
	v_cmp_gt_f32_e64 s[98:99], v166, v159
	v_cndmask_b32_e64 v164, 0, 1, s[16:17]
	v_addc_co_u32_e32 v164, vcc, v172, v164, vcc
	v_cmp_gt_f32_e32 vcc, v167, v159
	v_cndmask_b32_e64 v165, 0, 1, s[98:99]
	s_nop 0
	v_addc_co_u32_e32 v164, vcc, v164, v165, vcc
	s_waitcnt lgkmcnt(0)
	v_cmp_gt_f32_e64 s[16:17], v168, v159
	v_cmp_gt_f32_e32 vcc, v169, v159
	s_nop 0
	v_cndmask_b32_e64 v165, 0, 1, s[16:17]
	v_addc_co_u32_e32 v168, vcc, v164, v165, vcc
	ds_read_b128 v[164:167], v154 offset:1328
	v_cmp_gt_f32_e64 s[16:17], v170, v159
	v_cmp_gt_f32_e32 vcc, v171, v159
	s_nop 0
	v_cndmask_b32_e64 v169, 0, 1, s[16:17]
	v_addc_co_u32_e32 v172, vcc, v168, v169, vcc
	ds_read_b128 v[168:171], v154 offset:1344
	s_waitcnt lgkmcnt(1)
	v_cmp_gt_f32_e64 s[16:17], v164, v159
	v_cmp_gt_f32_e32 vcc, v165, v159
	v_cmp_gt_f32_e64 s[98:99], v166, v159
	v_cndmask_b32_e64 v164, 0, 1, s[16:17]
	v_addc_co_u32_e32 v164, vcc, v172, v164, vcc
	v_cmp_gt_f32_e32 vcc, v167, v159
	v_cndmask_b32_e64 v165, 0, 1, s[98:99]
	s_nop 0
	v_addc_co_u32_e32 v164, vcc, v164, v165, vcc
	s_waitcnt lgkmcnt(0)
	v_cmp_gt_f32_e64 s[16:17], v168, v159
	v_cmp_gt_f32_e32 vcc, v169, v159
	s_nop 0
	v_cndmask_b32_e64 v165, 0, 1, s[16:17]
	v_addc_co_u32_e32 v168, vcc, v164, v165, vcc
	ds_read_b128 v[164:167], v154 offset:1360
	v_cmp_gt_f32_e64 s[16:17], v170, v159
	v_cmp_gt_f32_e32 vcc, v171, v159
	s_nop 0
	v_cndmask_b32_e64 v169, 0, 1, s[16:17]
	v_addc_co_u32_e32 v172, vcc, v168, v169, vcc
	ds_read_b128 v[168:171], v154 offset:1376
	s_waitcnt lgkmcnt(1)
	v_cmp_gt_f32_e64 s[16:17], v164, v159
	v_cmp_gt_f32_e32 vcc, v165, v159
	v_cmp_gt_f32_e64 s[98:99], v166, v159
	v_cndmask_b32_e64 v164, 0, 1, s[16:17]
	v_addc_co_u32_e32 v164, vcc, v172, v164, vcc
	v_cmp_gt_f32_e32 vcc, v167, v159
	v_cndmask_b32_e64 v165, 0, 1, s[98:99]
	s_nop 0
	v_addc_co_u32_e32 v164, vcc, v164, v165, vcc
	s_waitcnt lgkmcnt(0)
	v_cmp_gt_f32_e64 s[16:17], v168, v159
	v_cmp_gt_f32_e32 vcc, v169, v159
	s_nop 0
	v_cndmask_b32_e64 v165, 0, 1, s[16:17]
	v_addc_co_u32_e32 v168, vcc, v164, v165, vcc
	ds_read_b128 v[164:167], v154 offset:1392
	v_cmp_gt_f32_e64 s[16:17], v170, v159
	v_cmp_gt_f32_e32 vcc, v171, v159
	s_nop 0
	v_cndmask_b32_e64 v169, 0, 1, s[16:17]
	v_addc_co_u32_e32 v172, vcc, v168, v169, vcc
	ds_read_b128 v[168:171], v154 offset:1408
	s_waitcnt lgkmcnt(1)
	v_cmp_gt_f32_e64 s[16:17], v164, v159
	v_cmp_gt_f32_e32 vcc, v165, v159
	v_cmp_gt_f32_e64 s[98:99], v166, v159
	v_cndmask_b32_e64 v164, 0, 1, s[16:17]
	v_addc_co_u32_e32 v164, vcc, v172, v164, vcc
	v_cmp_gt_f32_e32 vcc, v167, v159
	v_cndmask_b32_e64 v165, 0, 1, s[98:99]
	s_nop 0
	v_addc_co_u32_e32 v164, vcc, v164, v165, vcc
	s_waitcnt lgkmcnt(0)
	v_cmp_gt_f32_e64 s[16:17], v168, v159
	v_cmp_gt_f32_e32 vcc, v169, v159
	s_nop 0
	v_cndmask_b32_e64 v165, 0, 1, s[16:17]
	v_addc_co_u32_e32 v168, vcc, v164, v165, vcc
	ds_read_b128 v[164:167], v154 offset:1424
	v_cmp_gt_f32_e64 s[16:17], v170, v159
	v_cmp_gt_f32_e32 vcc, v171, v159
	s_nop 0
	v_cndmask_b32_e64 v169, 0, 1, s[16:17]
	v_addc_co_u32_e32 v172, vcc, v168, v169, vcc
	ds_read_b128 v[168:171], v154 offset:1440
	s_waitcnt lgkmcnt(1)
	v_cmp_gt_f32_e64 s[16:17], v164, v159
	v_cmp_gt_f32_e32 vcc, v165, v159
	v_cmp_gt_f32_e64 s[98:99], v166, v159
	v_cndmask_b32_e64 v164, 0, 1, s[16:17]
	v_addc_co_u32_e32 v164, vcc, v172, v164, vcc
	v_cmp_gt_f32_e32 vcc, v167, v159
	v_cndmask_b32_e64 v165, 0, 1, s[98:99]
	s_nop 0
	v_addc_co_u32_e32 v164, vcc, v164, v165, vcc
	s_waitcnt lgkmcnt(0)
	v_cmp_gt_f32_e64 s[16:17], v168, v159
	v_cmp_gt_f32_e32 vcc, v169, v159
	s_nop 0
	v_cndmask_b32_e64 v165, 0, 1, s[16:17]
	v_addc_co_u32_e32 v168, vcc, v164, v165, vcc
	ds_read_b128 v[164:167], v154 offset:1456
	v_cmp_gt_f32_e64 s[16:17], v170, v159
	v_cmp_gt_f32_e32 vcc, v171, v159
	s_nop 0
	v_cndmask_b32_e64 v169, 0, 1, s[16:17]
	v_addc_co_u32_e32 v172, vcc, v168, v169, vcc
	ds_read_b128 v[168:171], v154 offset:1472
	s_waitcnt lgkmcnt(1)
	v_cmp_gt_f32_e64 s[16:17], v164, v159
	v_cmp_gt_f32_e32 vcc, v165, v159
	v_cmp_gt_f32_e64 s[98:99], v166, v159
	v_cndmask_b32_e64 v164, 0, 1, s[16:17]
	v_addc_co_u32_e32 v164, vcc, v172, v164, vcc
	v_cmp_gt_f32_e32 vcc, v167, v159
	v_cndmask_b32_e64 v165, 0, 1, s[98:99]
	s_nop 0
	v_addc_co_u32_e32 v164, vcc, v164, v165, vcc
	s_waitcnt lgkmcnt(0)
	v_cmp_gt_f32_e64 s[16:17], v168, v159
	v_cmp_gt_f32_e32 vcc, v169, v159
	s_nop 0
	v_cndmask_b32_e64 v165, 0, 1, s[16:17]
	v_addc_co_u32_e32 v164, vcc, v164, v165, vcc
	s_nop 0
	s_nop 0
	s_nop 0
	s_nop 0
	v_cmp_gt_u32_e32 vcc, 16, v164
	v_add_u32_e32 v164, 16, v164
	s_and_b64 vcc, s[4:5], vcc
	v_cndmask_b32_e32 v168, v151, v164, vcc
	ds_read_b128 v[164:167], v154 offset:1536
	v_lshlrev_b32_e32 v168, 2, v168
	ds_permute_b32 v159, v168, v159
	ds_permute_b32 v158, v168, v158
	ds_read_b128 v[168:171], v154 offset:1552
	s_waitcnt lgkmcnt(3)
	v_cmp_gt_f32_e32 vcc, v165, v157
	s_waitcnt lgkmcnt(2)
	v_cndmask_b32_e64 v159, v163, v159, s[46:47]
	v_cndmask_b32_e64 v165, 0, 1, vcc
	v_cmp_gt_f32_e32 vcc, v164, v157
	s_waitcnt lgkmcnt(1)
	v_cndmask_b32_e64 v158, v160, v158, s[46:47]
	v_addc_co_u32_e32 v164, vcc, 0, v165, vcc
	v_cmp_gt_f32_e64 s[16:17], v166, v157
	v_cmp_gt_f32_e32 vcc, v167, v157
	s_nop 0
	v_cndmask_b32_e64 v165, 0, 1, s[16:17]
	v_addc_co_u32_e32 v164, vcc, v164, v165, vcc
	s_waitcnt lgkmcnt(0)
	v_cmp_gt_f32_e64 s[16:17], v168, v157
	v_cmp_gt_f32_e32 vcc, v169, v157
	s_nop 0
	v_cndmask_b32_e64 v165, 0, 1, s[16:17]
	v_addc_co_u32_e32 v168, vcc, v164, v165, vcc
	ds_read_b128 v[164:167], v154 offset:1568
	v_cmp_gt_f32_e64 s[16:17], v170, v157
	v_cmp_gt_f32_e32 vcc, v171, v157
	s_nop 0
	v_cndmask_b32_e64 v169, 0, 1, s[16:17]
	v_addc_co_u32_e32 v172, vcc, v168, v169, vcc
	ds_read_b128 v[168:171], v154 offset:1584
	s_waitcnt lgkmcnt(1)
	v_cmp_gt_f32_e64 s[16:17], v164, v157
	v_cmp_gt_f32_e32 vcc, v165, v157
	v_cmp_gt_f32_e64 s[98:99], v166, v157
	v_cndmask_b32_e64 v164, 0, 1, s[16:17]
	v_addc_co_u32_e32 v164, vcc, v172, v164, vcc
	v_cmp_gt_f32_e32 vcc, v167, v157
	v_cndmask_b32_e64 v165, 0, 1, s[98:99]
	s_nop 0
	v_addc_co_u32_e32 v164, vcc, v164, v165, vcc
	s_waitcnt lgkmcnt(0)
	v_cmp_gt_f32_e64 s[16:17], v168, v157
	v_cmp_gt_f32_e32 vcc, v169, v157
	s_nop 0
	v_cndmask_b32_e64 v165, 0, 1, s[16:17]
	v_addc_co_u32_e32 v168, vcc, v164, v165, vcc
	ds_read_b128 v[164:167], v154 offset:1600
	v_cmp_gt_f32_e64 s[16:17], v170, v157
	v_cmp_gt_f32_e32 vcc, v171, v157
	s_nop 0
	v_cndmask_b32_e64 v169, 0, 1, s[16:17]
	v_addc_co_u32_e32 v172, vcc, v168, v169, vcc
	ds_read_b128 v[168:171], v154 offset:1616
	s_waitcnt lgkmcnt(1)
	v_cmp_gt_f32_e64 s[16:17], v164, v157
	v_cmp_gt_f32_e32 vcc, v165, v157
	v_cmp_gt_f32_e64 s[98:99], v166, v157
	v_cndmask_b32_e64 v164, 0, 1, s[16:17]
	v_addc_co_u32_e32 v164, vcc, v172, v164, vcc
	v_cmp_gt_f32_e32 vcc, v167, v157
	v_cndmask_b32_e64 v165, 0, 1, s[98:99]
	s_nop 0
	v_addc_co_u32_e32 v164, vcc, v164, v165, vcc
	s_waitcnt lgkmcnt(0)
	v_cmp_gt_f32_e64 s[16:17], v168, v157
	v_cmp_gt_f32_e32 vcc, v169, v157
	s_nop 0
	v_cndmask_b32_e64 v165, 0, 1, s[16:17]
	v_addc_co_u32_e32 v168, vcc, v164, v165, vcc
	ds_read_b128 v[164:167], v154 offset:1632
	v_cmp_gt_f32_e64 s[16:17], v170, v157
	v_cmp_gt_f32_e32 vcc, v171, v157
	s_nop 0
	v_cndmask_b32_e64 v169, 0, 1, s[16:17]
	v_addc_co_u32_e32 v172, vcc, v168, v169, vcc
	ds_read_b128 v[168:171], v154 offset:1648
	s_waitcnt lgkmcnt(1)
	v_cmp_gt_f32_e64 s[16:17], v164, v157
	v_cmp_gt_f32_e32 vcc, v165, v157
	v_cmp_gt_f32_e64 s[98:99], v166, v157
	v_cndmask_b32_e64 v164, 0, 1, s[16:17]
	v_addc_co_u32_e32 v164, vcc, v172, v164, vcc
	v_cmp_gt_f32_e32 vcc, v167, v157
	v_cndmask_b32_e64 v165, 0, 1, s[98:99]
	s_nop 0
	v_addc_co_u32_e32 v164, vcc, v164, v165, vcc
	s_waitcnt lgkmcnt(0)
	v_cmp_gt_f32_e64 s[16:17], v168, v157
	v_cmp_gt_f32_e32 vcc, v169, v157
	s_nop 0
	v_cndmask_b32_e64 v165, 0, 1, s[16:17]
	v_addc_co_u32_e32 v168, vcc, v164, v165, vcc
	ds_read_b128 v[164:167], v154 offset:1664
	v_cmp_gt_f32_e64 s[16:17], v170, v157
	v_cmp_gt_f32_e32 vcc, v171, v157
	s_nop 0
	v_cndmask_b32_e64 v169, 0, 1, s[16:17]
	v_addc_co_u32_e32 v172, vcc, v168, v169, vcc
	ds_read_b128 v[168:171], v154 offset:1680
	s_waitcnt lgkmcnt(1)
	v_cmp_gt_f32_e64 s[16:17], v164, v157
	v_cmp_gt_f32_e32 vcc, v165, v157
	v_cmp_gt_f32_e64 s[98:99], v166, v157
	v_cndmask_b32_e64 v164, 0, 1, s[16:17]
	v_addc_co_u32_e32 v164, vcc, v172, v164, vcc
	v_cmp_gt_f32_e32 vcc, v167, v157
	v_cndmask_b32_e64 v165, 0, 1, s[98:99]
	s_nop 0
	v_addc_co_u32_e32 v164, vcc, v164, v165, vcc
	s_waitcnt lgkmcnt(0)
	v_cmp_gt_f32_e64 s[16:17], v168, v157
	v_cmp_gt_f32_e32 vcc, v169, v157
	s_nop 0
	v_cndmask_b32_e64 v165, 0, 1, s[16:17]
	v_addc_co_u32_e32 v168, vcc, v164, v165, vcc
	ds_read_b128 v[164:167], v154 offset:1696
	v_cmp_gt_f32_e64 s[16:17], v170, v157
	v_cmp_gt_f32_e32 vcc, v171, v157
	s_nop 0
	v_cndmask_b32_e64 v169, 0, 1, s[16:17]
	v_addc_co_u32_e32 v172, vcc, v168, v169, vcc
	ds_read_b128 v[168:171], v154 offset:1712
	s_waitcnt lgkmcnt(1)
	v_cmp_gt_f32_e64 s[16:17], v164, v157
	v_cmp_gt_f32_e32 vcc, v165, v157
	v_cmp_gt_f32_e64 s[98:99], v166, v157
	v_cndmask_b32_e64 v164, 0, 1, s[16:17]
	v_addc_co_u32_e32 v164, vcc, v172, v164, vcc
	v_cmp_gt_f32_e32 vcc, v167, v157
	v_cndmask_b32_e64 v165, 0, 1, s[98:99]
	s_nop 0
	v_addc_co_u32_e32 v164, vcc, v164, v165, vcc
	s_waitcnt lgkmcnt(0)
	v_cmp_gt_f32_e64 s[16:17], v168, v157
	v_cmp_gt_f32_e32 vcc, v169, v157
	s_nop 0
	v_cndmask_b32_e64 v165, 0, 1, s[16:17]
	v_addc_co_u32_e32 v168, vcc, v164, v165, vcc
	ds_read_b128 v[164:167], v154 offset:1728
	v_cmp_gt_f32_e64 s[16:17], v170, v157
	v_cmp_gt_f32_e32 vcc, v171, v157
	s_nop 0
	v_cndmask_b32_e64 v169, 0, 1, s[16:17]
	v_addc_co_u32_e32 v172, vcc, v168, v169, vcc
	ds_read_b128 v[168:171], v154 offset:1792
	s_waitcnt lgkmcnt(1)
	v_cmp_gt_f32_e64 s[16:17], v164, v157
	v_cmp_gt_f32_e32 vcc, v165, v157
	s_nop 0
	v_cndmask_b32_e64 v164, 0, 1, s[16:17]
	v_addc_co_u32_e32 v164, vcc, v172, v164, vcc
	s_nop 0
	s_nop 0
	s_nop 0
	s_nop 0
	v_cmp_gt_u32_e32 vcc, 16, v164
	v_add_u32_e32 v164, 32, v164
	s_and_b64 vcc, s[4:5], vcc
	v_cndmask_b32_e32 v164, v152, v164, vcc
	v_lshlrev_b32_e32 v164, 2, v164
	ds_permute_b32 v157, v164, v157
	s_waitcnt lgkmcnt(1)
	v_cmp_gt_f32_e32 vcc, v169, v153
	ds_permute_b32 v155, v164, v155
	ds_read_b128 v[164:167], v154 offset:1808
	s_waitcnt lgkmcnt(2)
	v_cndmask_b32_e64 v157, v159, v157, s[48:49]
	v_cndmask_b32_e64 v159, 0, 1, vcc
	v_cmp_gt_f32_e32 vcc, v168, v153
	s_waitcnt lgkmcnt(1)
	v_cndmask_b32_e64 v155, v158, v155, s[48:49]
	v_addc_co_u32_e32 v159, vcc, 0, v159, vcc
	v_cmp_gt_f32_e32 vcc, v170, v153
	s_nop 1
	v_cndmask_b32_e64 v160, 0, 1, vcc
	v_cmp_gt_f32_e32 vcc, v171, v153
	ds_read_b128 v[168:171], v154 offset:1824
	s_nop 0
	v_addc_co_u32_e32 v159, vcc, v159, v160, vcc
	s_waitcnt lgkmcnt(1)
	v_cmp_gt_f32_e64 s[16:17], v164, v153
	v_cmp_gt_f32_e32 vcc, v165, v153
	s_nop 0
	v_cndmask_b32_e64 v160, 0, 1, s[16:17]
	v_addc_co_u32_e32 v159, vcc, v159, v160, vcc
	v_cmp_gt_f32_e32 vcc, v166, v153
	s_nop 1
	v_cndmask_b32_e64 v160, 0, 1, vcc
	v_cmp_gt_f32_e32 vcc, v167, v153
	ds_read_b128 v[164:167], v154 offset:1840
	s_nop 0
	v_addc_co_u32_e32 v159, vcc, v159, v160, vcc
	s_waitcnt lgkmcnt(1)
	v_cmp_gt_f32_e64 s[16:17], v168, v153
	v_cmp_gt_f32_e32 vcc, v169, v153
	s_nop 0
	v_cndmask_b32_e64 v160, 0, 1, s[16:17]
	v_addc_co_u32_e32 v159, vcc, v159, v160, vcc
	v_cmp_gt_f32_e32 vcc, v170, v153
	s_nop 1
	v_cndmask_b32_e64 v160, 0, 1, vcc
	v_cmp_gt_f32_e32 vcc, v171, v153
	ds_read_b128 v[168:171], v154 offset:1856
	s_nop 0
	v_addc_co_u32_e32 v159, vcc, v159, v160, vcc
	s_waitcnt lgkmcnt(1)
	v_cmp_gt_f32_e64 s[16:17], v164, v153
	v_cmp_gt_f32_e32 vcc, v165, v153
	s_nop 0
	v_cndmask_b32_e64 v160, 0, 1, s[16:17]
	v_addc_co_u32_e32 v159, vcc, v159, v160, vcc
	v_cmp_gt_f32_e32 vcc, v166, v153
	s_nop 1
	v_cndmask_b32_e64 v160, 0, 1, vcc
	v_cmp_gt_f32_e32 vcc, v167, v153
	ds_read_b128 v[164:167], v154 offset:1872
	s_nop 0
	v_addc_co_u32_e32 v159, vcc, v159, v160, vcc
	s_waitcnt lgkmcnt(1)
	v_cmp_gt_f32_e64 s[16:17], v168, v153
	v_cmp_gt_f32_e32 vcc, v169, v153
	s_nop 0
	v_cndmask_b32_e64 v160, 0, 1, s[16:17]
	v_addc_co_u32_e32 v159, vcc, v159, v160, vcc
	v_cmp_gt_f32_e32 vcc, v170, v153
	s_nop 1
	v_cndmask_b32_e64 v160, 0, 1, vcc
	v_cmp_gt_f32_e32 vcc, v171, v153
	ds_read_b128 v[168:171], v154 offset:1888
	s_nop 0
	v_addc_co_u32_e32 v159, vcc, v159, v160, vcc
	s_waitcnt lgkmcnt(1)
	v_cmp_gt_f32_e64 s[16:17], v164, v153
	v_cmp_gt_f32_e32 vcc, v165, v153
	s_nop 0
	v_cndmask_b32_e64 v160, 0, 1, s[16:17]
	v_addc_co_u32_e32 v159, vcc, v159, v160, vcc
	v_cmp_gt_f32_e32 vcc, v166, v153
	s_nop 1
	v_cndmask_b32_e64 v160, 0, 1, vcc
	v_cmp_gt_f32_e32 vcc, v167, v153
	ds_read_b128 v[164:167], v154 offset:1904
	s_nop 0
	v_addc_co_u32_e32 v159, vcc, v159, v160, vcc
	s_waitcnt lgkmcnt(1)
	v_cmp_gt_f32_e64 s[16:17], v168, v153
	v_cmp_gt_f32_e32 vcc, v169, v153
	s_nop 0
	v_cndmask_b32_e64 v160, 0, 1, s[16:17]
	v_addc_co_u32_e32 v159, vcc, v159, v160, vcc
	v_cmp_gt_f32_e32 vcc, v170, v153
	s_nop 1
	v_cndmask_b32_e64 v160, 0, 1, vcc
	v_cmp_gt_f32_e32 vcc, v171, v153
	ds_read_b128 v[168:171], v154 offset:1920
	s_nop 0
	v_addc_co_u32_e32 v159, vcc, v159, v160, vcc
	s_waitcnt lgkmcnt(1)
	v_cmp_gt_f32_e64 s[16:17], v164, v153
	v_cmp_gt_f32_e32 vcc, v165, v153
	s_nop 0
	v_cndmask_b32_e64 v160, 0, 1, s[16:17]
	v_addc_co_u32_e32 v159, vcc, v159, v160, vcc
	v_cmp_gt_f32_e32 vcc, v166, v153
	s_nop 1
	v_cndmask_b32_e64 v160, 0, 1, vcc
	v_cmp_gt_f32_e32 vcc, v167, v153
	ds_read_b128 v[164:167], v154 offset:1936
	s_nop 0
	v_addc_co_u32_e32 v159, vcc, v159, v160, vcc
	s_waitcnt lgkmcnt(1)
	v_cmp_gt_f32_e64 s[16:17], v168, v153
	v_cmp_gt_f32_e32 vcc, v169, v153
	s_nop 0
	v_cndmask_b32_e64 v160, 0, 1, s[16:17]
	v_addc_co_u32_e32 v159, vcc, v159, v160, vcc
	v_cmp_gt_f32_e32 vcc, v170, v153
	s_nop 1
	v_cndmask_b32_e64 v160, 0, 1, vcc
	v_cmp_gt_f32_e32 vcc, v171, v153
	ds_read_b128 v[168:171], v154 offset:1952
	s_nop 0
	v_addc_co_u32_e32 v159, vcc, v159, v160, vcc
	s_waitcnt lgkmcnt(1)
	v_cmp_gt_f32_e64 s[16:17], v164, v153
	v_cmp_gt_f32_e32 vcc, v165, v153
	s_nop 0
	v_cndmask_b32_e64 v160, 0, 1, s[16:17]
	v_addc_co_u32_e32 v159, vcc, v159, v160, vcc
	v_cmp_gt_f32_e32 vcc, v166, v153
	s_nop 1
	v_cndmask_b32_e64 v160, 0, 1, vcc
	v_cmp_gt_f32_e32 vcc, v167, v153
	ds_read_b128 v[164:167], v154 offset:1968
	s_nop 0
	v_addc_co_u32_e32 v159, vcc, v159, v160, vcc
	s_waitcnt lgkmcnt(1)
	v_cmp_gt_f32_e64 s[16:17], v168, v153
	v_cmp_gt_f32_e32 vcc, v169, v153
	s_nop 0
	v_cndmask_b32_e64 v160, 0, 1, s[16:17]
	v_addc_co_u32_e32 v159, vcc, v159, v160, vcc
	v_cmp_gt_f32_e32 vcc, v170, v153
	s_nop 1
	v_cndmask_b32_e64 v160, 0, 1, vcc
	v_cmp_gt_f32_e32 vcc, v171, v153
	ds_read_b128 v[168:171], v154 offset:1984
	s_nop 0
	v_addc_co_u32_e32 v159, vcc, v159, v160, vcc
	s_waitcnt lgkmcnt(1)
	v_cmp_gt_f32_e32 vcc, v164, v153
	v_max_f32_e32 v160, v162, v162
	s_nop 0
	v_cndmask_b32_e64 v154, 0, 1, vcc
	v_cmp_gt_f32_e32 vcc, v165, v153
	s_nop 1
	v_addc_co_u32_e32 v154, vcc, v159, v154, vcc
	v_cmp_gt_f32_e64 s[16:17], v166, v153
	v_cmp_gt_f32_e32 vcc, v167, v153
	s_nop 0
	v_cndmask_b32_e64 v159, 0, 1, s[16:17]
	v_addc_co_u32_e32 v154, vcc, v154, v159, vcc
	s_waitcnt lgkmcnt(0)
	v_cmp_gt_f32_e64 s[16:17], v168, v153
	v_cmp_gt_f32_e32 vcc, v169, v153
	s_nop 0
	v_cndmask_b32_e64 v159, 0, 1, s[16:17]
	v_addc_co_u32_e32 v154, vcc, v154, v159, vcc
	s_nop 0
	s_nop 0
	s_nop 0
	s_nop 0
	v_mov_b32_e32 v159, v201
	v_cmp_gt_u32_e32 vcc, 16, v154
	v_add_u32_e32 v154, 48, v154
	v_mov_b32_dpp v159, v162 row_ror:1 row_mask:0xf bank_mask:0xf
	v_max_f32_e32 v159, v159, v159
	v_max_f32_e32 v159, v160, v159
	s_nop 0
	s_and_b64 vcc, s[4:5], vcc
	v_cndmask_b32_e32 v154, v140, v154, vcc
	v_max_f32_dpp v159, v159, v159 row_ror:2 row_mask:0xf bank_mask:0xf
	s_nop 0
	s_nop 0
	s_nop 0
	v_lshlrev_b32_e32 v154, 2, v154
	ds_permute_b32 v153, v154, v153
	v_max_f32_dpp v159, v159, v159 row_ror:4 row_mask:0xf bank_mask:0xf
	s_nop 0
	s_nop 0
	s_nop 0
	ds_permute_b32 v154, v154, v156
	s_waitcnt lgkmcnt(1)
	v_cndmask_b32_e64 v153, v157, v153, s[50:51]
	v_max_f32_dpp v159, v159, v159 row_ror:8 row_mask:0xf bank_mask:0xf
	s_nop 0
	s_nop 0
	v_sub_f32_e32 v159, v162, v159
	v_mul_f32_e32 v159, 0x3fb8aa3b, v159
	v_exp_f32_e32 v159, v159
	s_waitcnt lgkmcnt(0)
	v_cndmask_b32_e64 v158, v155, v154, s[50:51]
	v_add_f32_dpp v156, v159, v159 row_ror:1 row_mask:0xf bank_mask:0xf bound_ctrl:1
	s_nop 1
	v_add_f32_dpp v156, v156, v156 row_ror:2 row_mask:0xf bank_mask:0xf bound_ctrl:1
	s_nop 1
	v_add_f32_dpp v156, v156, v156 row_ror:4 row_mask:0xf bank_mask:0xf bound_ctrl:1
	s_nop 1
	v_add_f32_dpp v156, v156, v156 row_ror:8 row_mask:0xf bank_mask:0xf bound_ctrl:1
	v_div_scale_f32 v160, s[80:81], v156, v156, v159
	v_rcp_f32_e32 v162, v160
	s_mov_b32 s80, 0x31200000
	v_fma_f32 v154, -v160, v162, 1.0
	v_fmac_f32_e32 v162, v154, v162
	v_div_scale_f32 v154, vcc, v159, v156, v159
	v_mul_f32_e32 v155, v154, v162
	v_fma_f32 v157, -v160, v155, v154
	v_fmac_f32_e32 v155, v157, v162
	v_fma_f32 v154, -v160, v155, v154
	v_mov_b32_e32 v157, v201
	v_div_fmas_f32 v154, v154, v162, v155
	v_div_fixup_f32 v156, v154, v156, v159
	v_mov_b32_dpp v157, v153 row_ror:1 row_mask:0xf bank_mask:0xf
	v_max_f32_e32 v159, v153, v153
	v_max_f32_e32 v157, v157, v157
	v_max_f32_e32 v157, v159, v157
	s_nop 0
	v_lshl_add_u64 v[154:155], s[92:93], 0, v[132:133]
	v_add_co_u32_e32 v154, vcc, s80, v154
	v_max_f32_dpp v157, v157, v157 row_ror:2 row_mask:0xf bank_mask:0xf
	s_nop 0
	s_nop 0
	s_nop 0
	v_addc_co_u32_e32 v155, vcc, 0, v155, vcc
	s_nop 0
	v_max_f32_dpp v157, v157, v157 row_ror:4 row_mask:0xf bank_mask:0xf
	s_nop 0
	s_nop 0
	s_nop 0
	global_store_dword v[154:155], v156, off
	s_nop 0
	v_max_f32_dpp v157, v157, v157 row_ror:8 row_mask:0xf bank_mask:0xf
	s_nop 0
	s_nop 0
	v_sub_f32_e32 v153, v153, v157
	v_mul_f32_e32 v153, 0x3fb8aa3b, v153
	v_exp_f32_e32 v153, v153
	s_nop 1
	v_add_f32_dpp v156, v153, v153 row_ror:1 row_mask:0xf bank_mask:0xf bound_ctrl:1
	s_nop 1
	v_add_f32_dpp v156, v156, v156 row_ror:2 row_mask:0xf bank_mask:0xf bound_ctrl:1
	s_nop 1
	v_add_f32_dpp v156, v156, v156 row_ror:4 row_mask:0xf bank_mask:0xf bound_ctrl:1
	s_nop 1
	v_add_f32_dpp v159, v156, v156 row_ror:8 row_mask:0xf bank_mask:0xf bound_ctrl:1
	v_div_scale_f32 v160, s[80:81], v159, v159, v153
	v_rcp_f32_e32 v162, v160
	v_lshl_add_u64 v[156:157], s[92:93], 0, v[134:135]
	global_store_dword v[156:157], v161, off
	v_fma_f32 v156, -v160, v162, 1.0
	v_fmac_f32_e32 v162, v156, v162
	v_div_scale_f32 v156, vcc, v153, v159, v153
	v_mul_f32_e32 v157, v156, v162
	v_fma_f32 v161, -v160, v157, v156
	v_fmac_f32_e32 v157, v161, v162
	v_fma_f32 v156, -v160, v157, v156
	v_div_fmas_f32 v156, v156, v162, v157
	v_div_fixup_f32 v153, v156, v159, v153
	global_store_dword v[154:155], v153, off offset:256
	v_lshlrev_b32_e32 v153, 7, v158
	v_lshl_add_u64 v[154:155], s[92:93], 0, v[136:137]
	s_and_b64 vcc, exec, s[52:53]
	global_store_dword v[154:155], v153, off
	s_cbranch_vccnz .LBB0_1847
	v_readlane_b32 s10, v254, 10
	v_readlane_b32 s11, v254, 11
	s_andn2_b64 vcc, exec, s[10:11]
	s_cbranch_vccnz .LBB0_1871
	global_load_dwordx4 v[164:167], v[112:113], off
	global_load_dwordx4 v[168:171], v[112:113], off offset:16
	global_load_dwordx4 v[172:175], v[112:113], off offset:32
	global_load_dwordx4 v[176:179], v[112:113], off offset:48
	global_load_dwordx4 v[180:183], v[114:115], off
	global_load_dwordx4 v[184:187], v[116:117], off
	global_load_dwordx4 v[188:191], v[118:119], off
	global_load_dwordx4 v[192:195], v[120:121], off
	s_waitcnt vmcnt(0)
	v_pk_mul_f32 v[46:47], v[46:47], v[166:167]
	v_pk_mul_f32 v[44:45], v[44:45], v[164:165]
	v_pk_mul_f32 v[42:43], v[42:43], v[170:171]
	v_pk_mul_f32 v[40:41], v[40:41], v[168:169]
	v_pk_mul_f32 v[38:39], v[38:39], v[174:175]
	v_pk_mul_f32 v[36:37], v[36:37], v[172:173]
	v_pk_mul_f32 v[34:35], v[34:35], v[178:179]
	v_pk_mul_f32 v[32:33], v[32:33], v[176:177]
	v_pk_mul_f32 v[50:51], v[50:51], v[182:183]
	v_pk_mul_f32 v[48:49], v[48:49], v[180:181]
	v_pk_mul_f32 v[62:63], v[62:63], v[186:187]
	v_pk_mul_f32 v[60:61], v[60:61], v[184:185]
	v_pk_mul_f32 v[58:59], v[58:59], v[190:191]
	v_pk_mul_f32 v[56:57], v[56:57], v[188:189]
	v_pk_mul_f32 v[54:55], v[54:55], v[194:195]
	v_pk_mul_f32 v[52:53], v[52:53], v[192:193]
